# speedup vs baseline: 1.0136x; 1.0136x over previous
_Z12front_kernel9FrontArgs8PrepArgs8FragArgs:
	s_load_dwordx16 s[4:19], s[0:1], 0x10
	s_cmpk_gt_i32 s2, 0xff
	s_mov_b64 s[20:21], -1
	s_cbranch_scc0 .LBB1_117
	s_load_dword s3, s[0:1], 0x164
	s_add_u32 s34, s0, 0x60
	s_addc_u32 s35, s1, 0
	s_add_i32 s30, s2, 0xffffff00
	s_waitcnt lgkmcnt(0)
	s_add_i32 s20, s3, 0x1ff
	s_ashr_i32 s21, s20, 31
	s_lshr_b32 s21, s21, 23
	s_add_i32 s20, s20, s21
	s_ashr_i32 s22, s20, 9
	s_cmp_ge_i32 s30, s22
	s_mov_b64 s[20:21], -1
	s_cbranch_scc0 .LBB1_103
	s_load_dword s31, s[0:1], 0x2f4
	s_add_u32 s24, s0, 0x1b0
	s_addc_u32 s25, s1, 0
	s_sub_i32 s33, s30, s22
	s_waitcnt lgkmcnt(0)
	s_add_i32 s20, s31, 7
	s_ashr_i32 s21, s20, 31
	s_lshr_b32 s21, s21, 29
	s_add_i32 s20, s20, s21
	s_ashr_i32 s26, s20, 3
	s_cmp_ge_i32 s33, s26
	s_mov_b64 s[20:21], -1
	s_cbranch_scc0 .LBB1_89
	s_cmp_lg_u32 s33, s26
	s_cbranch_scc0 .LBB1_61
	s_not_b32 s26, s26
	s_add_i32 s38, s33, s26
	s_cmpk_lt_u32 s38, 0x100
	s_cselect_b64 s[28:29], -1, 0
	s_cmpk_gt_u32 s38, 0xff
	s_load_dwordx4 s[20:23], s[0:1], 0x50
	s_cselect_b64 s[26:27], -1, 0
	s_and_b64 s[36:37], s[28:29], exec
	s_cselect_b32 s5, s5, s7
	s_cselect_b32 s4, s4, s6
	s_bfe_u32 s36, s38, 0x20006
	s_lshl_b32 s6, s38, 5
	v_lshrrev_b32_e32 v4, 5, v0
	s_and_b32 s37, s6, 0x7e0
	v_and_b32_e32 v5, 31, v0
	s_mul_i32 s6, s36, 0x180
	v_lshrrev_b32_e32 v4, 5, v0
	v_and_b32_e32 v5, 31, v0
	v_add_u32_e32 v6, s6, v4
	v_lshlrev_b32_e32 v6, 11, v6
	v_add3_u32 v6, v6, s37, v5
	v_lshlrev_b32_e32 v6, 2, v6
	v_mul_u32_u24_e32 v7, 33, v4
	v_add_lshl_u32 v7, v7, v5, 2
	s_mov_b64 s[38:39], s[4:5]
	s_and_b64 s[4:5], s[28:29], exec
	v_and_b32_e32 v31, 63, v0
	s_cselect_b32 s7, s9, s13
	s_cselect_b32 s6, s8, s12
	v_lshlrev_b32_e32 v2, 2, v31
	s_cselect_b32 s5, s11, s15
	s_cselect_b32 s4, s10, s14
	global_load_dword v32, v2, s[6:7]
	global_load_dword v33, v2, s[4:5]
	global_load_dword v27, v2, s[6:7] offset:512
	global_load_dword v24, v2, s[6:7] offset:768
	global_load_dword v23, v2, s[6:7] offset:1024
	global_load_dword v1, v2, s[6:7] offset:1280
	global_load_dword v29, v2, s[6:7] offset:256
	global_load_dword v30, v2, s[4:5] offset:256
	global_load_dword v28, v2, s[4:5] offset:512
	global_load_dword v26, v2, s[4:5] offset:768
	global_load_dword v25, v2, s[4:5] offset:1024
	global_load_dword v22, v2, s[4:5] offset:1280
	global_load_dword v36, v6, s[38:39] nt
	s_add_u32 s38, s38, 0x20000
	s_addc_u32 s39, s39, 0
	global_load_dword v37, v6, s[38:39] nt
	s_add_u32 s38, s38, 0x20000
	s_addc_u32 s39, s39, 0
	global_load_dword v38, v6, s[38:39] nt
	s_add_u32 s38, s38, 0x20000
	s_addc_u32 s39, s39, 0
	global_load_dword v39, v6, s[38:39] nt
	s_add_u32 s38, s38, 0x20000
	s_addc_u32 s39, s39, 0
	global_load_dword v40, v6, s[38:39] nt
	s_add_u32 s38, s38, 0x20000
	s_addc_u32 s39, s39, 0
	global_load_dword v41, v6, s[38:39] nt
	s_add_u32 s38, s38, 0x20000
	s_addc_u32 s39, s39, 0
	global_load_dword v42, v6, s[38:39] nt
	s_add_u32 s38, s38, 0x20000
	s_addc_u32 s39, s39, 0
	global_load_dword v43, v6, s[38:39] nt
	s_add_u32 s38, s38, 0x20000
	s_addc_u32 s39, s39, 0
	global_load_dword v44, v6, s[38:39] nt
	s_add_u32 s38, s38, 0x20000
	s_addc_u32 s39, s39, 0
	global_load_dword v45, v6, s[38:39] nt
	s_add_u32 s38, s38, 0x20000
	s_addc_u32 s39, s39, 0
	global_load_dword v46, v6, s[38:39] nt
	s_add_u32 s38, s38, 0x20000
	s_addc_u32 s39, s39, 0
	global_load_dword v47, v6, s[38:39] nt
	s_add_u32 s38, s38, 0x20000
	s_addc_u32 s39, s39, 0
	global_load_dword v48, v6, s[38:39] nt
	s_add_u32 s38, s38, 0x20000
	s_addc_u32 s39, s39, 0
	global_load_dword v49, v6, s[38:39] nt
	s_add_u32 s38, s38, 0x20000
	s_addc_u32 s39, s39, 0
	global_load_dword v50, v6, s[38:39] nt
	s_add_u32 s38, s38, 0x20000
	s_addc_u32 s39, s39, 0
	global_load_dword v51, v6, s[38:39] nt
	s_add_u32 s38, s38, 0x20000
	s_addc_u32 s39, s39, 0
	global_load_dword v52, v6, s[38:39] nt
	s_add_u32 s38, s38, 0x20000
	s_addc_u32 s39, s39, 0
	global_load_dword v53, v6, s[38:39] nt
	s_add_u32 s38, s38, 0x20000
	s_addc_u32 s39, s39, 0
	global_load_dword v54, v6, s[38:39] nt
	s_add_u32 s38, s38, 0x20000
	s_addc_u32 s39, s39, 0
	global_load_dword v55, v6, s[38:39] nt
	s_add_u32 s38, s38, 0x20000
	s_addc_u32 s39, s39, 0
	global_load_dword v56, v6, s[38:39] nt
	s_add_u32 s38, s38, 0x20000
	s_addc_u32 s39, s39, 0
	global_load_dword v57, v6, s[38:39] nt
	s_add_u32 s38, s38, 0x20000
	s_addc_u32 s39, s39, 0
	global_load_dword v58, v6, s[38:39] nt
	s_add_u32 s38, s38, 0x20000
	s_addc_u32 s39, s39, 0
	global_load_dword v59, v6, s[38:39] nt
	s_waitcnt vmcnt(23)
	ds_write_b32 v7, v36
	s_waitcnt vmcnt(22)
	ds_write_b32 v7, v37 offset:2112
	s_waitcnt vmcnt(21)
	ds_write_b32 v7, v38 offset:4224
	s_waitcnt vmcnt(20)
	ds_write_b32 v7, v39 offset:6336
	s_waitcnt vmcnt(19)
	ds_write_b32 v7, v40 offset:8448
	s_waitcnt vmcnt(18)
	ds_write_b32 v7, v41 offset:10560
	s_waitcnt vmcnt(17)
	ds_write_b32 v7, v42 offset:12672
	s_waitcnt vmcnt(16)
	ds_write_b32 v7, v43 offset:14784
	s_waitcnt vmcnt(15)
	ds_write_b32 v7, v44 offset:16896
	s_waitcnt vmcnt(14)
	ds_write_b32 v7, v45 offset:19008
	s_waitcnt vmcnt(13)
	ds_write_b32 v7, v46 offset:21120
	s_waitcnt vmcnt(12)
	ds_write_b32 v7, v47 offset:23232
	s_waitcnt vmcnt(11)
	ds_write_b32 v7, v48 offset:25344
	s_waitcnt vmcnt(10)
	ds_write_b32 v7, v49 offset:27456
	s_waitcnt vmcnt(9)
	ds_write_b32 v7, v50 offset:29568
	s_waitcnt vmcnt(8)
	ds_write_b32 v7, v51 offset:31680
	s_waitcnt vmcnt(7)
	ds_write_b32 v7, v52 offset:33792
	s_waitcnt vmcnt(6)
	ds_write_b32 v7, v53 offset:35904
	s_waitcnt vmcnt(5)
	ds_write_b32 v7, v54 offset:38016
	s_waitcnt vmcnt(4)
	ds_write_b32 v7, v55 offset:40128
	s_waitcnt vmcnt(3)
	ds_write_b32 v7, v56 offset:42240
	s_waitcnt vmcnt(2)
	ds_write_b32 v7, v57 offset:44352
	s_waitcnt vmcnt(1)
	ds_write_b32 v7, v58 offset:46464
	s_waitcnt vmcnt(0)
	ds_write_b32 v7, v59 offset:48576
	s_and_b64 s[40:41], s[28:29], exec
	s_waitcnt lgkmcnt(0)
	s_barrier
	v_lshrrev_b32_e32 v34, 4, v0
	v_and_b32_e32 v35, 28, v34
	v_lshlrev_b32_e32 v37, 2, v35
	s_movk_i32 s4, 0x84
	v_mad_u32_u24 v2, v31, s4, v37
	ds_read2st64_b32 v[12:13], v2 offset1:33
	ds_read2st64_b32 v[8:9], v2 offset0:66 offset1:99
	ds_read2st64_b32 v[6:7], v2 offset0:132 offset1:165
	v_mov_b32_e32 v3, 0
	s_cselect_b32 s5, s19, s21
	s_waitcnt lgkmcnt(2)
	v_add_f32_e32 v2, 0, v12
	v_add_f32_e32 v2, v2, v13
	s_waitcnt lgkmcnt(1)
	v_add_f32_e32 v2, v2, v8
	v_add_f32_e32 v2, v2, v9
	s_waitcnt lgkmcnt(0)
	v_add_f32_e32 v2, v2, v6
	v_add_f32_e32 v2, v2, v7
	v_mov_b32_e32 v10, v9
	v_mov_b32_e32 v11, v8
	v_add_f32_dpp v2, v2, v2 quad_perm:[1,0,3,2] row_mask:0xf bank_mask:0xf bound_ctrl:1
	s_nop 1
	v_add_f32_dpp v2, v2, v2 quad_perm:[2,3,0,1] row_mask:0xf bank_mask:0xf bound_ctrl:1
	s_nop 1
	v_add_f32_dpp v2, v2, v2 row_half_mirror row_mask:0xf bank_mask:0xf bound_ctrl:1
	s_nop 1
	v_add_f32_dpp v2, v2, v2 row_mirror row_mask:0xf bank_mask:0xf bound_ctrl:1
	s_nop 0
	v_readlane_b32 s4, v2, 16
	v_readlane_b32 s8, v2, 48
	v_readlane_b32 s6, v2, 0
	v_readlane_b32 s7, v2, 32
	v_mov_b32_e32 v4, s4
	v_mov_b32_e32 v5, s8
	v_pk_add_f32 v[4:5], s[6:7], v[4:5]
	s_nop 0
	v_add_f32_e32 v2, v4, v5
	v_mul_f32_e32 v2, 0x3b2aaaab, v2
	v_pk_add_f32 v[4:5], v[12:13], v[2:3] op_sel_hi:[1,0] neg_lo:[0,1] neg_hi:[0,1]
	v_pk_add_f32 v[16:17], v[10:11], v[2:3] op_sel_hi:[1,0] neg_lo:[0,1] neg_hi:[0,1]
	v_pk_mul_f32 v[14:15], v[4:5], v[4:5]
	v_mov_b32_e32 v10, v7
	v_mov_b32_e32 v11, v6
	v_pk_mul_f32 v[18:19], v[16:17], v[16:17]
	v_pk_add_f32 v[10:11], v[10:11], v[2:3] op_sel_hi:[1,0] neg_lo:[0,1] neg_hi:[0,1]
	v_add_f32_e32 v2, v14, v15
	v_add_f32_e32 v2, v19, v2
	v_pk_mul_f32 v[20:21], v[10:11], v[10:11]
	v_add_f32_e32 v2, v18, v2
	v_add_f32_e32 v2, v21, v2
	v_add_f32_e32 v2, v20, v2
	s_nop 1
	v_add_f32_dpp v2, v2, v2 quad_perm:[1,0,3,2] row_mask:0xf bank_mask:0xf bound_ctrl:1
	s_nop 1
	v_add_f32_dpp v2, v2, v2 quad_perm:[2,3,0,1] row_mask:0xf bank_mask:0xf bound_ctrl:1
	s_nop 1
	v_add_f32_dpp v2, v2, v2 row_half_mirror row_mask:0xf bank_mask:0xf bound_ctrl:1
	s_nop 1
	v_add_f32_dpp v2, v2, v2 row_mirror row_mask:0xf bank_mask:0xf bound_ctrl:1
	s_nop 0
	v_readlane_b32 s4, v2, 16
	v_readlane_b32 s8, v2, 48
	v_readlane_b32 s6, v2, 0
	v_readlane_b32 s7, v2, 32
	v_mov_b32_e32 v14, s4
	v_mov_b32_e32 v15, s8
	v_pk_add_f32 v[14:15], s[6:7], v[14:15]
	s_mov_b32 s4, 0x800000
	v_add_f32_e32 v2, v14, v15
	v_mov_b32_e32 v14, 0x3727c5ac
	v_fmac_f32_e32 v14, 0x3b2aaaab, v2
	v_mul_f32_e32 v2, 0x4b800000, v14
	v_cmp_gt_f32_e32 vcc, s4, v14
	s_cselect_b32 s4, s18, s20
	s_lshl_b32 s6, s36, 11
	v_cndmask_b32_e32 v2, v14, v2, vcc
	v_rsq_f32_e32 v2, v2
	s_or_b32 s8, s6, s37
	v_mul_f32_e32 v14, 0x45800000, v2
	v_cndmask_b32_e32 v36, v2, v14, vcc
	v_add_u32_e32 v2, s8, v35
	v_mul_u32_u24_e32 v18, 0x180, v2
	v_mul_f32_e32 v2, v4, v36
	s_waitcnt vmcnt(10)
	v_fma_f32 v2, v32, v2, v33
	v_cvt_pk_bf16_f32 v4, v2, s0
	v_or_b32_e32 v2, v18, v31
	v_lshl_add_u64 v[14:15], v[2:3], 1, s[4:5]
	global_store_short v[14:15], v4, off
	s_and_b64 vcc, exec, s[26:27]
	v_mul_f32_e32 v20, v5, v36
	v_lshlrev_b32_e32 v14, 1, v18
	v_lshlrev_b32_e32 v4, 1, v31
	v_add_u32_e32 v18, v18, v31
	s_cbranch_vccz .LBB1_10
	s_waitcnt vmcnt(5)
	v_fma_f32 v5, v29, v20, v30
	v_mov_b32_e32 v15, v3
	v_cvt_pk_bf16_f32 v19, v5, s0
	v_lshl_add_u64 v[38:39], s[20:21], 0, v[14:15]
	v_mov_b32_e32 v5, v3
	v_lshl_add_u64 v[38:39], v[38:39], 0, v[4:5]
	global_store_short v[38:39], v19, off offset:128
	v_mov_b32_e32 v19, v3
	s_mov_b64 s[6:7], 0
	s_branch .LBB1_11
